# speedup vs baseline: 1.0505x; 1.0110x over previous
_Z10cvt_kernelPKfPDF16_lS0_S1_lS0_S1_lS0_S1_lS0_S1_lPjS0_Pf:
	s_cmpk_lt_u32 s2, 0x80
	s_cbranch_scc1 .Lcvt_orig
	s_cmpk_ge_u32 s2, 0x1000
	s_cbranch_scc1 .Lcvt_orig
	v_lshlrev_b32_e32 v1, 5, v0
	v_lshlrev_b32_e32 v2, 4, v0
	s_cmpk_ge_u32 s2, 0x800
	s_cbranch_scc1 .Lcvt_fw
	s_load_dwordx4 s[4:7], s[0:1], 0x0
	s_lshl_b32 s8, s2, 13
	s_lshl_b32 s9, s2, 12
	s_waitcnt lgkmcnt(0)
	s_add_u32 s4, s4, s8
	s_addc_u32 s5, s5, 0
	s_add_u32 s6, s6, s9
	s_addc_u32 s7, s7, 0
	global_load_dwordx4 v[4:7], v1, s[4:5] nt
	global_load_dwordx4 v[8:11], v1, s[4:5] offset:16 nt
	s_waitcnt vmcnt(1)
	v_cvt_pk_f16_f32 v12, v4, v5
	v_cvt_pk_f16_f32 v13, v6, v7
	s_waitcnt vmcnt(0)
	v_cvt_pk_f16_f32 v14, v8, v9
	v_cvt_pk_f16_f32 v15, v10, v11
	global_store_dwordx4 v2, v[12:15], s[6:7]
	s_endpgm
.Lcvt_fw:
	s_load_dwordx4 s[4:7], s[0:1], 0x18
	s_sub_u32 s3, s2, 0x800
	s_lshl_b32 s8, s3, 13
	s_lshl_b32 s9, s3, 12
	s_mov_b32 s10, 0x41800000
	s_mov_b32 s11, 0x41800000
	s_waitcnt lgkmcnt(0)
	s_add_u32 s4, s4, s8
	s_addc_u32 s5, s5, 0
	s_add_u32 s6, s6, s9
	s_addc_u32 s7, s7, 0
	global_load_dwordx4 v[4:7], v1, s[4:5] nt
	global_load_dwordx4 v[8:11], v1, s[4:5] offset:16 nt
	s_waitcnt vmcnt(1)
	v_pk_mul_f32 v[4:5], v[4:5], s[10:11]
	v_pk_mul_f32 v[6:7], v[6:7], s[10:11]
	s_waitcnt vmcnt(0)
	v_pk_mul_f32 v[8:9], v[8:9], s[10:11]
	v_pk_mul_f32 v[10:11], v[10:11], s[10:11]
	v_cvt_pk_f16_f32 v12, v4, v5
	v_cvt_pk_f16_f32 v13, v6, v7
	v_cvt_pk_f16_f32 v14, v8, v9
	v_cvt_pk_f16_f32 v15, v10, v11
	global_store_dwordx4 v2, v[12:15], s[6:7]
	s_endpgm
.Lcvt_orig:
	s_load_dwordx16 s[4:19], s[0:1], 0x40
	s_cmp_eq_u32 s2, 0
	s_cselect_b64 s[20:21], -1, 0
	v_cmp_gt_u32_e32 vcc, 64, v0
	s_and_b64 s[22:23], s[20:21], vcc
	s_and_saveexec_b64 s[20:21], s[22:23]
	s_cbranch_execnz .LBB0_22
	s_or_b64 exec, exec, s[20:21]
	s_cmpk_lt_u32 s2, 0x80
	s_waitcnt lgkmcnt(0)
	s_mov_b64 s[18:19], -1
	s_cbranch_scc0 .LBB0_23
